# code placement: moe2 K-loop moved 8 bytes relative to moe1 (2 s_nop ahead of its header, 2 fewer ahead of the attention phase so the attention loops keep their offsets)
# baseline (speedup 1.0000x reference)
; template <class Epi, class Sched, bool ALIGN_EPI, bool FP8 = false>
; __device__ __forceinline__ void gemm_phase(LAS unsigned char* lds, const bf16_t* A, const bf16_t* Bt, const int K, const Sched& S, const Epi& E, const int wave_in) {
;     ...
; #pragma unroll
;         for (int a = 0; a < 2; ++a)
; #pragma unroll
;             for (int b = 0; b < 2; ++b)
; #pragma unroll
;                 for (int m = 0; m < 4; ++m)
; #pragma unroll
;                     for (int n = 0; n < 2; ++n) acc[a][b][m][n] = (f32x4){0.f, 0.f, 0.f, 0.f};
;         cur = nxt; cB = nB; ++ui;
; #pragma unroll
;         for (int h = 0; h < 2; ++h)
; #pragma unroll
;             for (int i = 0; i < 2; ++i) vA[h][i] = vN[h][i];
.LBB0_1138:
	s_add_u32 s0, s10, 0x100
	v_mov_b32_e32 v34, 0
	s_addc_u32 s1, s11, 0
	s_mov_b32 s89, -2
	s_mov_b64 s[14:15], s[76:77]
	v_mov_b32_e32 v35, 0
	v_mov_b64_e32 v[36:37], 0
	v_mov_b64_e32 v[38:39], 0
	v_mov_b64_e32 v[40:41], 0
	v_mov_b64_e32 v[50:51], 0
	v_mov_b64_e32 v[52:53], 0
	v_mov_b64_e32 v[54:55], 0
	v_mov_b64_e32 v[56:57], 0
	v_mov_b64_e32 v[66:67], 0
	v_mov_b64_e32 v[68:69], 0
	v_mov_b64_e32 v[70:71], 0
	v_mov_b64_e32 v[72:73], 0
	v_mov_b64_e32 v[82:83], 0
	v_mov_b64_e32 v[84:85], 0
	v_mov_b64_e32 v[86:87], 0
	v_mov_b64_e32 v[88:89], 0
	v_mov_b64_e32 v[42:43], 0
	v_mov_b64_e32 v[44:45], 0
	v_mov_b64_e32 v[46:47], 0
	v_mov_b64_e32 v[48:49], 0
	v_mov_b64_e32 v[58:59], 0
	v_mov_b64_e32 v[60:61], 0
	v_mov_b64_e32 v[62:63], 0
	v_mov_b64_e32 v[64:65], 0
	v_mov_b64_e32 v[74:75], 0
	v_mov_b64_e32 v[76:77], 0
	v_mov_b64_e32 v[78:79], 0
	v_mov_b64_e32 v[80:81], 0
	v_mov_b64_e32 v[90:91], 0
	v_mov_b64_e32 v[92:93], 0
	v_mov_b64_e32 v[94:95], 0
	v_mov_b64_e32 v[96:97], 0
	v_mov_b64_e32 v[98:99], 0
	v_mov_b64_e32 v[100:101], 0
	v_mov_b64_e32 v[102:103], 0
	v_mov_b64_e32 v[104:105], 0
	v_mov_b64_e32 v[114:115], 0
	v_mov_b64_e32 v[116:117], 0
	v_mov_b64_e32 v[118:119], 0
	v_mov_b64_e32 v[120:121], 0
	v_mov_b64_e32 v[130:131], 0
	v_mov_b64_e32 v[132:133], 0
	v_mov_b64_e32 v[134:135], 0
	v_mov_b64_e32 v[136:137], 0
	v_mov_b64_e32 v[148:149], 0
	v_mov_b64_e32 v[150:151], 0
	v_mov_b64_e32 v[152:153], 0
	v_mov_b64_e32 v[154:155], 0
	v_mov_b64_e32 v[106:107], 0
	v_mov_b64_e32 v[108:109], 0
	v_mov_b64_e32 v[110:111], 0
	v_mov_b64_e32 v[112:113], 0
	v_mov_b64_e32 v[122:123], 0
	v_mov_b64_e32 v[124:125], 0
	v_mov_b64_e32 v[126:127], 0
	v_mov_b64_e32 v[128:129], 0
	v_mov_b64_e32 v[138:139], 0
	v_mov_b64_e32 v[140:141], 0
	v_mov_b64_e32 v[142:143], 0
	v_mov_b64_e32 v[144:145], 0
	v_mov_b64_e32 v[156:157], 0
	v_mov_b64_e32 v[158:159], 0
	v_mov_b64_e32 v[160:161], 0
	v_mov_b64_e32 v[162:163], 0
	s_nop 0
	s_nop 0

; #define INP(k) inp_ptr(k)
; __device__ __forceinline__ void attn_phase(Frame& F) {
;     const bf16_t* Q = (const bf16_t*)(F.ws + WS_R1 + R1_Q); const bf16_t* Kb = (const bf16_t*)(F.ws + WS_R1 + R1_K); const bf16_t* Vb = (const bf16_t*)(F.ws + WS_R1 + R1_V);
;     bf16_t* O = (bf16_t*)(F.ws + WS_R1 + R1_O); const unsigned char* V8 = F.ws + WS_R1 + R1_V8;
;     float lam;
;     { const float* lp = INP(IN_DLAM); const float a = wave_sum(lp[F.lane] * lp[64 + F.lane]), b = wave_sum(lp[128 + F.lane] * lp[192 + F.lane]); lam = expf(a) - expf(b) + LAM_INIT; }
;     const float* subg = INP(IN_DSUBG);
;     const int bx = F.bid; const int vcu = (F.G % 8 == 0) ? (bx % 8) * (F.G / 8) + bx / 8 : bx;
;     i32x8 qfu = i32x8{};
;     for (int id = vcu; id < 4096; id += F.G) {
.LBB0_1286:
	s_nop 0
	s_nop 0
	s_nop 0
	s_nop 0
	s_nop 0
	s_nop 0
	s_nop 0
	s_nop 0
	s_nop 0
	s_nop 0
	s_nop 0
	s_nop 0
	s_or_b64 exec, exec, s[2:3]
	s_mov_b32 s0, s53
	s_waitcnt lgkmcnt(0)
	s_barrier
	s_mov_b32 s8, s90
	s_mov_b32 s9, s73
	s_mov_b64 s[74:75], s[94:95]
	s_mov_b64 s[0:1], s[88:89]
	v_mbcnt_lo_u32_b32 v0, -1, 0
	v_mbcnt_hi_u32_b32 v0, -1, v0
	s_load_dwordx2 s[0:1], s[0:1], 0x78
	v_and_b32_e32 v0, 63, v0
	v_lshlrev_b32_e32 v3, 2, v0
	s_waitcnt lgkmcnt(0)
	global_load_dword v0, v3, s[0:1]
	global_load_dword v2, v3, s[0:1] offset:256
	s_waitcnt vmcnt(0)
	v_mul_f32_e32 v4, v0, v2
	ds_swizzle_b32 v4, v4 offset:swizzle(SWAP,1)
	s_waitcnt lgkmcnt(0)
	v_fmac_f32_e32 v4, v0, v2
	ds_swizzle_b32 v0, v4 offset:swizzle(SWAP,2)
	s_waitcnt lgkmcnt(0)
	v_add_f32_e32 v0, v4, v0
	global_load_dword v4, v3, s[0:1] offset:512
	s_nop 0
	global_load_dword v3, v3, s[0:1] offset:768
	ds_swizzle_b32 v2, v0 offset:swizzle(SWAP,4)
	s_mov_b64 s[0:1], s[88:89]
	s_load_dwordx2 s[4:5], s[0:1], 0x80
	s_and_b32 s0, s8, 7
	s_waitcnt lgkmcnt(0)
	v_add_f32_e32 v0, v0, v2
	ds_swizzle_b32 v2, v0 offset:swizzle(SWAP,8)
	s_cmp_lg_u32 s0, 0
	s_waitcnt lgkmcnt(0)
	v_add_f32_e32 v0, v0, v2
	ds_swizzle_b32 v2, v0 offset:swizzle(SWAP,16)
	s_waitcnt lgkmcnt(0)
	v_add_f32_e32 v0, v0, v2
	v_mov_b32_e32 v2, v0
	s_nop 1
	v_permlane32_swap_b32_e32 v0, v2
	s_waitcnt vmcnt(0)
	v_mul_f32_e32 v5, v4, v3
	ds_swizzle_b32 v5, v5 offset:swizzle(SWAP,1)
	s_waitcnt lgkmcnt(0)
	v_fmac_f32_e32 v5, v4, v3
	ds_swizzle_b32 v3, v5 offset:swizzle(SWAP,2)
	s_waitcnt lgkmcnt(0)
	v_add_f32_e32 v3, v5, v3
	ds_swizzle_b32 v4, v3 offset:swizzle(SWAP,4)
	s_waitcnt lgkmcnt(0)
	v_add_f32_e32 v3, v3, v4
	ds_swizzle_b32 v4, v3 offset:swizzle(SWAP,8)
	s_waitcnt lgkmcnt(0)
	v_add_f32_e32 v3, v3, v4
	ds_swizzle_b32 v4, v3 offset:swizzle(SWAP,16)
	s_waitcnt lgkmcnt(0)
	v_add_f32_e32 v3, v3, v4
	v_mov_b32_e32 v4, v3
	s_nop 1
	v_permlane32_swap_b32_e32 v3, v4
	s_cbranch_scc0 .LBB0_1288
	s_cmpk_gt_i32 s9, 0xfff
	s_cbranch_scc0 .LBB0_1289
	s_branch .LBB0_1362
